# split re-tuned to 115 converter workgroups (141 GEMM workgroups still need 20 rounds; fewer tiles per converter), otherwise as the 112-converter version
# speedup vs baseline: 1.0158x; 1.0066x over previous
.LBB0_839:
	s_add_u32 s16, s56, 0x3eb00000
	s_addc_u32 s17, s57, 0
	s_cmp_lt_i32 s58, 8
	s_cselect_b64 s[0:1], -1, 0
	s_cmp_gt_i32 s59, 7
	s_cselect_b64 s[2:3], -1, 0
	s_and_b64 s[0:1], s[0:1], s[2:3]
	s_andn2_b64 vcc, exec, s[0:1]
	s_cbranch_vccnz .LBB0_921
	s_mov_b32 s99, s13
	s_cmp_lt_u32 s12, 141
	s_cbranch_scc1 .Lsp7_gemm
	s_mov_b32 s98, s12
	s_add_i32 s12, s12, -77
	s_mov_b32 s13, 115
	v_lshrrev_b32_e32 v140, 3, v0
	s_add_u32 s0, s94, 0xffffffe0
	s_addc_u32 s1, s95, -1
	s_load_dwordx2 s[52:53], s[0:1], 0x0
	s_waitcnt lgkmcnt(0)
	s_branch .Lcv_364
.Lsp7_gemm:
	s_mov_b32 s13, 141
	s_cmpk_gt_i32 s12, 0xaff
	v_readfirstlane_b32 s3, v0
	s_cbranch_scc1 .LBB0_867
	v_lshlrev_b32_e32 v2, 4, v0
	v_and_b32_e32 v3, 32, v0
	v_bitop3_b32 v2, v2, v3, 48 bitop3:0x6c
	v_lshrrev_b32_e32 v3, 1, v0
	v_lshrrev_b32_e32 v5, 5, v0
	v_and_b32_e32 v3, 24, v3
	v_and_b32_e32 v5, 4, v5
	s_waitcnt vmcnt(14)
	v_bfe_u32 v6, v0, 2, 2
	v_bfe_u32 v4, v0, 2, 4
	v_or3_b32 v3, v5, v6, v3
	v_lshrrev_b32_e32 v5, 3, v0
	v_and_or_b32 v2, v0, 64, v2
	v_and_or_b32 v6, v5, 48, v4
	v_and_or_b32 v5, v5, 32, v3
	s_lshr_b32 s6, s3, 6
	v_lshl_or_b32 v202, v5, 11, v2
	v_bfe_u32 v5, v0, 3, 25
	s_lshr_b32 s14, s3, 8
	s_lshl_b32 s10, s6, 10
	v_or_b32_e32 v5, 64, v5
	s_movk_i32 s0, 0x70
	s_add_u32 s11, s56, 0x4db00000
	v_and_or_b32 v4, v5, s0, v4
	s_movk_i32 s0, 0x60
	s_addc_u32 s18, s57, 0
	s_ashr_i32 s19, s12, 31
	v_and_or_b32 v3, v5, s0, v3
	s_lshr_b32 s0, s19, 29
	s_add_i32 s0, s12, s0
	s_ashr_i32 s1, s0, 3
	s_and_b32 s0, s0, -8
	s_sub_i32 s0, s12, s0
	s_cmp_lt_i32 s0, 0
	s_movk_i32 s20, 0x161
	s_cselect_b32 s2, s20, 0x160
	s_mul_i32 s0, s0, s2
	s_add_i32 s0, s0, s1
	s_mul_hi_i32 s1, s0, 0x2e8ba2e9
	s_lshr_b32 s2, s1, 31
	s_ashr_i32 s1, s1, 6
	s_add_i32 s1, s1, s2
	s_lshl_b32 s4, s1, 3
	s_mulk_i32 s1, 0x160
	s_sub_i32 s0, s0, s1
	s_sext_i32_i16 s1, s0
	s_bfe_u32 s1, s1, 0x3001c
	s_add_i32 s1, s0, s1
	s_sext_i32_i16 s2, s1
	s_and_b32 s1, s1, 0xfff8
	s_sub_i32 s0, s0, s1
	s_sext_i32_i16 s0, s0
	s_add_i32 s0, s4, s0
	s_ashr_i32 s1, s0, 31
	s_lshr_b32 s2, s2, 3
	s_lshl_b64 s[4:5], s[0:1], 19
	s_add_u32 s26, s24, s4
	s_addc_u32 s27, s25, s5
	s_bfe_i64 s[4:5], s[2:3], 0x100000
	s_lshl_b64 s[4:5], s[4:5], 19
	s_add_u32 s8, s11, s4
	s_addc_u32 s9, s18, s5
	s_add_i32 s1, s10, 0
	v_lshl_or_b32 v201, v6, 11, v2
	v_lshl_or_b32 v203, v4, 11, v2
	v_lshl_or_b32 v204, v3, 11, v2
	s_mov_b64 s[4:5], s[8:9]
	s_add_i32 s21, s1, 0x10000
	v_mov_b32_e32 v2, v202
	s_mov_b32 m0, s21
	s_add_i32 s33, s1, 0x12000
	global_load_lds_dwordx4 v2, s[4:5]
	v_mov_b32_e32 v2, v204
	s_mov_b32 m0, s33
	s_mov_b32 s7, 0
	global_load_lds_dwordx4 v2, s[4:5]
	s_add_u32 s4, s8, 0x40000
	s_addc_u32 s5, s9, 0
	s_add_i32 s35, s1, 0x14000
	v_mov_b32_e32 v2, v202
	s_mov_b32 m0, s35
	s_add_i32 s60, s1, 0x16000
	global_load_lds_dwordx4 v2, s[4:5]
	v_mov_b32_e32 v2, v204
	s_mov_b32 m0, s60
	s_add_i32 s61, s1, 0x2000
	global_load_lds_dwordx4 v2, s[4:5]
	s_mov_b64 s[4:5], s[26:27]
	v_mov_b32_e32 v2, v201
	s_mov_b32 m0, s1
	s_nop 0
	global_load_lds_dwordx4 v2, s[4:5]
	v_mov_b32_e32 v2, v203
	s_mov_b32 m0, s61
	s_nop 0
	global_load_lds_dwordx4 v2, s[4:5]
	s_add_u32 s4, s26, 0x40000
	s_addc_u32 s5, s27, 0
	s_add_i32 s62, s1, 0x4000
	v_mov_b32_e32 v2, v201
	s_mov_b32 m0, s62
	s_add_i32 s63, s1, 0x6000
	global_load_lds_dwordx4 v2, s[4:5]
	v_mov_b32_e32 v2, v203
	s_mov_b32 m0, s63
	s_cmp_eq_u32 s14, 1
	global_load_lds_dwordx4 v2, s[4:5]
	s_cselect_b64 s[4:5], -1, 0
	s_cmp_lg_u32 s14, 1
	s_cbranch_scc1 .LBB0_843
	s_barrier
